# P6 epilogue (h1 = x + g1*acc): 8 X-row loads in flight per wave instead of serialized load-wait-store
# speedup vs baseline: 1.0034x; 1.0034x over previous
; #define PG8_STAGE(bufoff, gbase, voff) do { _Pragma("unroll") for (int _i = 0; _i < 2; ++_i) \
;         __builtin_amdgcn_global_load_lds((const unsigned*)((const char*)(gbase) + (voff)[_i]), (PG8_LAS unsigned*)(lds + (bufoff) + ldsw + _i * 8192), 16, 0, 0); } while (0)
; #define PG8_LDA(dst, b, h) do { _Pragma("unroll") for (int m = 0; m < 4; ++m) _Pragma("unroll") for (int k = 0; k < 2; ++k) dst[m][k] = *(const PG8_LAS bf16x8*)(lds + PG8_SA(b, h) + aoff + m * 2048 + k * 1024); } while (0)
; #define PG8_LDB(dst, b, h) do { _Pragma("unroll") for (int n = 0; n < 2; ++n) _Pragma("unroll") for (int k = 0; k < 2; ++k) dst[n][k] = *(const PG8_LAS bf16x8*)(lds + PG8_SB(b, h) + boff + n * 2048 + k * 1024); } while (0)
; #define PG8_WAIT_V(n) asm volatile("s_waitcnt vmcnt(" #n ")" ::: "memory")
; #define PG8_WAIT_L(n) asm volatile("s_waitcnt lgkmcnt(" #n ")" ::: "memory")
; #define PG8_BAR __builtin_amdgcn_s_barrier()
; #define PG8_SCHED __builtin_amdgcn_sched_barrier(0)
; template <class Epi, class Sched, bool ALIGN_EPI = false, bool SP2 = false, bool F8 = false, bool GATHER = false>
; __device__ __forceinline__ void gemm_phase(PG8_LAS unsigned char* lds, const Gemm g, const Sched& S, const Epi& E) {
;     ...
;             PG8_LDB(B0, 0, 0); PG8_LDB(B1, 0, 1); PG8_SCHED; PG8_LDA(At, 0, 0); PG8_STAGE(PG8_SA(1, 1), a1, vo[1]);
;             PG8_WAIT_V(8); PG8_WAIT_L(0); PG8_BAR; PG8_MMA(0, 0, At, B0); PG8_MMA(0, 1, At, B1); PG8_BAR; PG8_SCHED;
;             PG8_LDA(At, 0, 1); PG8_STAGE(PG8_SB(0, 0), b2, voffB); PG8_STAGE(PG8_SB(0, 1), b2 + hstep, voffB); PG8_STAGE(PG8_SA(0, 0), a2, s0);
;             PG8_WAIT_V(8); PG8_WAIT_L(0); PG8_BAR; PG8_MMA(1, 0, At, B0); PG8_MMA(1, 1, At, B1); PG8_BAR; PG8_SCHED;
.LBB0_123:
	ds_read_b128 v[26:29], v198
	ds_read_b128 v[30:33], v198 offset:1024
	ds_read_b128 v[18:21], v198 offset:2048
	ds_read_b128 v[22:25], v198 offset:3072
	ds_read_b128 v[10:13], v199
	ds_read_b128 v[14:17], v199 offset:1024
	ds_read_b128 v[2:5], v199 offset:2048
	ds_read_b128 v[6:9], v199 offset:3072
	s_add_u32 s65, s80, 0x80
	s_addc_u32 s66, s81, 0
	s_cmp_eq_u32 s64, 12
	s_cselect_b32 s85, s5, s66
	s_cselect_b32 s84, s7, s65
	s_cselect_b32 s83, s44, s53
	s_cselect_b32 s82, s51, s52
	v_lshl_add_u64 v[228:229], s[80:81], 0, v[180:181]
	s_add_i32 m0, s11, 0xc000
	ds_read_b128 v[186:189], v200
	ds_read_b128 v[190:193], v200 offset:1024
	ds_read_b128 v[204:207], v200 offset:2048
	ds_read_b128 v[208:211], v200 offset:3072
	ds_read_b128 v[212:215], v200 offset:4096
	ds_read_b128 v[216:219], v200 offset:5120
	ds_read_b128 v[220:223], v200 offset:6144
	ds_read_b128 v[224:227], v200 offset:7168
	global_load_lds_dwordx4 v[228:229], off
	v_lshl_add_u64 v[228:229], s[80:81], 0, v[178:179]
	s_add_i32 m0, s11, 0xe000
	s_nop 0
	global_load_lds_dwordx4 v[228:229], off
	s_waitcnt vmcnt(8)
	s_waitcnt lgkmcnt(0)
	s_barrier
	s_setprio 1
	s_waitcnt lgkmcnt(0)
	v_mfma_scale_f32_16x16x128_f8f6f4 v[158:161], v[26:33], v[186:193], v[158:161], v201, v201 op_sel_hi:[0,0,0]
	v_mfma_scale_f32_16x16x128_f8f6f4 v[154:157], v[18:25], v[186:193], v[154:157], v201, v201 op_sel_hi:[0,0,0]
	v_mfma_scale_f32_16x16x128_f8f6f4 v[142:145], v[26:33], v[204:211], v[142:145], v201, v201 op_sel_hi:[0,0,0]
	v_mfma_scale_f32_16x16x128_f8f6f4 v[138:141], v[18:25], v[204:211], v[138:141], v201, v201 op_sel_hi:[0,0,0]
	v_mfma_scale_f32_16x16x128_f8f6f4 v[126:129], v[26:33], v[212:219], v[126:129], v201, v201 op_sel_hi:[0,0,0]
	v_mfma_scale_f32_16x16x128_f8f6f4 v[122:125], v[18:25], v[212:219], v[122:125], v201, v201 op_sel_hi:[0,0,0]
	v_mfma_scale_f32_16x16x128_f8f6f4 v[110:113], v[26:33], v[220:227], v[110:113], v201, v201 op_sel_hi:[0,0,0]
	v_mfma_scale_f32_16x16x128_f8f6f4 v[106:109], v[18:25], v[220:227], v[106:109], v201, v201 op_sel_hi:[0,0,0]
	s_setprio 0
	s_setprio 1
	v_mfma_scale_f32_16x16x128_f8f6f4 v[150:153], v[10:17], v[186:193], v[150:153], v201, v201 op_sel_hi:[0,0,0]
	v_mfma_scale_f32_16x16x128_f8f6f4 v[146:149], v[2:9], v[186:193], v[146:149], v201, v201 op_sel_hi:[0,0,0]
	v_mfma_scale_f32_16x16x128_f8f6f4 v[134:137], v[10:17], v[204:211], v[134:137], v201, v201 op_sel_hi:[0,0,0]
	v_mfma_scale_f32_16x16x128_f8f6f4 v[130:133], v[2:9], v[204:211], v[130:133], v201, v201 op_sel_hi:[0,0,0]
	v_mfma_scale_f32_16x16x128_f8f6f4 v[118:121], v[10:17], v[212:219], v[118:121], v201, v201 op_sel_hi:[0,0,0]
	v_mfma_scale_f32_16x16x128_f8f6f4 v[114:117], v[2:9], v[212:219], v[114:117], v201, v201 op_sel_hi:[0,0,0]
	v_mfma_scale_f32_16x16x128_f8f6f4 v[102:105], v[10:17], v[220:227], v[102:105], v201, v201 op_sel_hi:[0,0,0]
	v_mfma_scale_f32_16x16x128_f8f6f4 v[98:101], v[2:9], v[220:227], v[98:101], v201, v201 op_sel_hi:[0,0,0]
	s_setprio 0
	s_barrier
	s_add_i32 s65, s40, s10
	v_lshl_add_u64 v[186:187], s[82:83], 0, v[164:165]
	s_mov_b32 m0, s65
	ds_read_b128 v[204:207], v200 offset:16384
	ds_read_b128 v[208:211], v200 offset:17408
	ds_read_b128 v[212:215], v200 offset:18432
	ds_read_b128 v[216:219], v200 offset:19456
	ds_read_b128 v[220:223], v200 offset:20480
	ds_read_b128 v[224:227], v200 offset:21504
	ds_read_b128 v[228:231], v200 offset:22528
	ds_read_b128 v[232:235], v200 offset:23552
	global_load_lds_dwordx4 v[186:187], off
	s_add_i32 m0, s65, 0x2000
	s_add_u32 s66, s82, 0x40000
	v_lshl_add_u64 v[188:189], s[82:83], 0, v[168:169]
	s_addc_u32 s67, s83, 0
	s_add_i32 s65, s41, s10
	global_load_lds_dwordx4 v[188:189], off
	v_lshl_add_u64 v[190:191], s[66:67], 0, v[164:165]
	s_mov_b32 m0, s65
	v_lshl_add_u64 v[192:193], s[84:85], 0, v[166:167]
	global_load_lds_dwordx4 v[190:191], off
	v_lshl_add_u64 v[190:191], s[66:67], 0, v[168:169]
	s_add_i32 m0, s65, 0x2000
	s_nop 0
	global_load_lds_dwordx4 v[190:191], off
	v_lshl_add_u64 v[190:191], s[84:85], 0, v[162:163]
	s_mov_b32 m0, s11
	s_nop 0
	global_load_lds_dwordx4 v[190:191], off
	s_mov_b32 m0, s33
	s_nop 0
	global_load_lds_dwordx4 v[192:193], off
	s_waitcnt vmcnt(8)
	s_waitcnt lgkmcnt(0)
	s_barrier
	s_setprio 1
	s_waitcnt lgkmcnt(0)
	v_mfma_scale_f32_16x16x128_f8f6f4 v[94:97], v[26:33], v[204:211], v[94:97], v201, v201 op_sel_hi:[0,0,0]
	v_mfma_scale_f32_16x16x128_f8f6f4 v[90:93], v[18:25], v[204:211], v[90:93], v201, v201 op_sel_hi:[0,0,0]
	v_mfma_scale_f32_16x16x128_f8f6f4 v[78:81], v[26:33], v[212:219], v[78:81], v201, v201 op_sel_hi:[0,0,0]
	v_mfma_scale_f32_16x16x128_f8f6f4 v[74:77], v[18:25], v[212:219], v[74:77], v201, v201 op_sel_hi:[0,0,0]
	v_mfma_scale_f32_16x16x128_f8f6f4 v[62:65], v[26:33], v[220:227], v[62:65], v201, v201 op_sel_hi:[0,0,0]
	v_mfma_scale_f32_16x16x128_f8f6f4 v[58:61], v[18:25], v[220:227], v[58:61], v201, v201 op_sel_hi:[0,0,0]
	v_mfma_scale_f32_16x16x128_f8f6f4 v[46:49], v[26:33], v[228:235], v[46:49], v201, v201 op_sel_hi:[0,0,0]
	v_mfma_scale_f32_16x16x128_f8f6f4 v[42:45], v[18:25], v[228:235], v[42:45], v201, v201 op_sel_hi:[0,0,0]
	s_setprio 0
	s_setprio 1
	v_mfma_scale_f32_16x16x128_f8f6f4 v[86:89], v[10:17], v[204:211], v[86:89], v201, v201 op_sel_hi:[0,0,0]
	v_mfma_scale_f32_16x16x128_f8f6f4 v[82:85], v[2:9], v[204:211], v[82:85], v201, v201 op_sel_hi:[0,0,0]
	v_mfma_scale_f32_16x16x128_f8f6f4 v[70:73], v[10:17], v[212:219], v[70:73], v201, v201 op_sel_hi:[0,0,0]
	v_mfma_scale_f32_16x16x128_f8f6f4 v[66:69], v[2:9], v[212:219], v[66:69], v201, v201 op_sel_hi:[0,0,0]
	v_mfma_scale_f32_16x16x128_f8f6f4 v[54:57], v[10:17], v[220:227], v[54:57], v201, v201 op_sel_hi:[0,0,0]
	v_mfma_scale_f32_16x16x128_f8f6f4 v[50:53], v[2:9], v[220:227], v[50:53], v201, v201 op_sel_hi:[0,0,0]
	v_mfma_scale_f32_16x16x128_f8f6f4 v[38:41], v[10:17], v[228:235], v[38:41], v201, v201 op_sel_hi:[0,0,0]
	v_mfma_scale_f32_16x16x128_f8f6f4 v[34:37], v[2:9], v[228:235], v[34:37], v201, v201 op_sel_hi:[0,0,0]
	s_setprio 0
	s_barrier
; #define PG8_STAGE(bufoff, gbase, voff) do { _Pragma("unroll") for (int _i = 0; _i < 2; ++_i) \
;         __builtin_amdgcn_global_load_lds((const unsigned*)((const char*)(gbase) + (voff)[_i]), (PG8_LAS unsigned*)(lds + (bufoff) + ldsw + _i * 8192), 16, 0, 0); } while (0)
; #define PG8_LDA(dst, b, h) do { _Pragma("unroll") for (int m = 0; m < 4; ++m) _Pragma("unroll") for (int k = 0; k < 2; ++k) dst[m][k] = *(const PG8_LAS bf16x8*)(lds + PG8_SA(b, h) + aoff + m * 2048 + k * 1024); } while (0)
; #define PG8_LDB(dst, b, h) do { _Pragma("unroll") for (int n = 0; n < 2; ++n) _Pragma("unroll") for (int k = 0; k < 2; ++k) dst[n][k] = *(const PG8_LAS bf16x8*)(lds + PG8_SB(b, h) + boff + n * 2048 + k * 1024); } while (0)
; #define PG8_WAIT_V(n) asm volatile("s_waitcnt vmcnt(" #n ")" ::: "memory")
; #define PG8_WAIT_L(n) asm volatile("s_waitcnt lgkmcnt(" #n ")" ::: "memory")
; #define PG8_BAR __builtin_amdgcn_s_barrier()
; #define PG8_SCHED __builtin_amdgcn_sched_barrier(0)
; template <class Epi, class Sched, bool ALIGN_EPI = false, bool SP2 = false, bool F8 = false, bool GATHER = false>
; __device__ __forceinline__ void gemm_phase(PG8_LAS unsigned char* lds, const Gemm g, const Sched& S, const Epi& E) {
;     ...
;             PG8_LDB(B0, 1, 0); PG8_LDB(B1, 1, 1); PG8_SCHED; PG8_LDA(At, 1, 0); PG8_STAGE(PG8_SA(0, 1), a2, s1);
;             PG8_WAIT_V(8); PG8_WAIT_L(0); PG8_BAR; PG8_MMA(0, 0, At, B0); PG8_MMA(0, 1, At, B1); PG8_BAR; PG8_SCHED;
;             PG8_LDA(At, 1, 1); PG8_STAGE(PG8_SB(1, 0), b3, voffB); PG8_STAGE(PG8_SB(1, 1), b3 + hstep, voffB); PG8_STAGE(PG8_SA(1, 0), a3, s0);
;             PG8_WAIT_V(8); PG8_WAIT_L(0); PG8_BAR; PG8_MMA(1, 0, At, B0); PG8_MMA(1, 1, At, B1); PG8_BAR; PG8_SCHED;
	s_add_i32 s65, 0, 0x18000
	s_add_i32 s68, 0, 0x1c000
	v_add_u32_e32 v14, s65, v196
	v_add_u32_e32 v30, s68, v196
	ds_read_b128 v[2:5], v14
	ds_read_b128 v[6:9], v14 offset:1024
	ds_read_b128 v[10:13], v14 offset:2048
	ds_read_b128 v[14:17], v14 offset:3072
	ds_read_b128 v[18:21], v30
	ds_read_b128 v[22:25], v30 offset:1024
	ds_read_b128 v[26:29], v30 offset:2048
	ds_read_b128 v[30:33], v30 offset:3072
	s_mov_b32 m0, s34
	v_lshl_add_u64 v[236:237], s[84:85], 0, v[170:171]
	ds_read_b128 v[204:207], v200 offset:32768
	ds_read_b128 v[208:211], v200 offset:33792
	ds_read_b128 v[212:215], v200 offset:34816
	ds_read_b128 v[216:219], v200 offset:35840
	ds_read_b128 v[220:223], v200 offset:36864
	ds_read_b128 v[224:227], v200 offset:37888
	ds_read_b128 v[228:231], v200 offset:38912
	ds_read_b128 v[232:235], v200 offset:39936
	global_load_lds_dwordx4 v[236:237], off
	v_lshl_add_u64 v[236:237], s[84:85], 0, v[172:173]
	s_mov_b32 m0, s35
	s_nop 0
	global_load_lds_dwordx4 v[236:237], off
	s_waitcnt vmcnt(8)
	s_waitcnt lgkmcnt(0)
	s_barrier
	s_setprio 1
	s_waitcnt lgkmcnt(0)
	v_mfma_scale_f32_16x16x128_f8f6f4 v[158:161], v[2:9], v[204:211], v[158:161], v201, v201 op_sel_hi:[0,0,0]
	v_mfma_scale_f32_16x16x128_f8f6f4 v[154:157], v[10:17], v[204:211], v[154:157], v201, v201 op_sel_hi:[0,0,0]
	v_mfma_scale_f32_16x16x128_f8f6f4 v[142:145], v[2:9], v[212:219], v[142:145], v201, v201 op_sel_hi:[0,0,0]
	v_mfma_scale_f32_16x16x128_f8f6f4 v[138:141], v[10:17], v[212:219], v[138:141], v201, v201 op_sel_hi:[0,0,0]
	v_mfma_scale_f32_16x16x128_f8f6f4 v[126:129], v[2:9], v[220:227], v[126:129], v201, v201 op_sel_hi:[0,0,0]
	v_mfma_scale_f32_16x16x128_f8f6f4 v[122:125], v[10:17], v[220:227], v[122:125], v201, v201 op_sel_hi:[0,0,0]
	v_mfma_scale_f32_16x16x128_f8f6f4 v[110:113], v[2:9], v[228:235], v[110:113], v201, v201 op_sel_hi:[0,0,0]
	v_mfma_scale_f32_16x16x128_f8f6f4 v[106:109], v[10:17], v[228:235], v[106:109], v201, v201 op_sel_hi:[0,0,0]
	s_setprio 0
	s_setprio 1
	v_mfma_scale_f32_16x16x128_f8f6f4 v[150:153], v[18:25], v[204:211], v[150:153], v201, v201 op_sel_hi:[0,0,0]
	v_mfma_scale_f32_16x16x128_f8f6f4 v[146:149], v[26:33], v[204:211], v[146:149], v201, v201 op_sel_hi:[0,0,0]
	v_mfma_scale_f32_16x16x128_f8f6f4 v[134:137], v[18:25], v[212:219], v[134:137], v201, v201 op_sel_hi:[0,0,0]
	v_mfma_scale_f32_16x16x128_f8f6f4 v[130:133], v[26:33], v[212:219], v[130:133], v201, v201 op_sel_hi:[0,0,0]
	v_mfma_scale_f32_16x16x128_f8f6f4 v[118:121], v[18:25], v[220:227], v[118:121], v201, v201 op_sel_hi:[0,0,0]
	v_mfma_scale_f32_16x16x128_f8f6f4 v[114:117], v[26:33], v[220:227], v[114:117], v201, v201 op_sel_hi:[0,0,0]
	v_mfma_scale_f32_16x16x128_f8f6f4 v[102:105], v[18:25], v[228:235], v[102:105], v201, v201 op_sel_hi:[0,0,0]
	v_mfma_scale_f32_16x16x128_f8f6f4 v[98:101], v[26:33], v[228:235], v[98:101], v201, v201 op_sel_hi:[0,0,0]
	s_setprio 0
	s_barrier
	s_add_i32 s65, s65, s10
	v_lshl_add_u64 v[186:187], v[186:187], 0, s[58:59]
	s_mov_b32 m0, s65
	ds_read_b128 v[204:207], v200 offset:49152
	ds_read_b128 v[208:211], v200 offset:50176
	ds_read_b128 v[212:215], v200 offset:51200
	ds_read_b128 v[216:219], v200 offset:52224
	ds_read_b128 v[220:223], v200 offset:53248
	ds_read_b128 v[224:227], v200 offset:54272
	ds_read_b128 v[228:231], v200 offset:55296
	ds_read_b128 v[232:235], v200 offset:56320
	global_load_lds_dwordx4 v[186:187], off
	s_add_i32 m0, s65, 0x2000
	s_add_u32 s66, s82, 0x40080
	v_lshl_add_u64 v[186:187], v[188:189], 0, s[58:59]
	s_addc_u32 s67, s83, 0
	s_add_i32 s65, s68, s10
	global_load_lds_dwordx4 v[186:187], off
	v_lshl_add_u64 v[186:187], s[66:67], 0, v[164:165]
	s_mov_b32 m0, s65
	s_nop 0
	global_load_lds_dwordx4 v[186:187], off
	v_lshl_add_u64 v[186:187], s[66:67], 0, v[168:169]
	s_add_i32 m0, s65, 0x2000
	s_nop 0
	global_load_lds_dwordx4 v[186:187], off
	v_lshl_add_u64 v[186:187], v[190:191], 0, s[58:59]
	s_mov_b32 m0, s36
	s_nop 0
	global_load_lds_dwordx4 v[186:187], off
	v_lshl_add_u64 v[186:187], v[192:193], 0, s[58:59]
	s_mov_b32 m0, s37
	s_nop 0
	global_load_lds_dwordx4 v[186:187], off
	s_waitcnt vmcnt(8)
	s_waitcnt lgkmcnt(0)
	s_barrier
	s_setprio 1
	s_waitcnt lgkmcnt(0)
	v_mfma_scale_f32_16x16x128_f8f6f4 v[94:97], v[2:9], v[204:211], v[94:97], v201, v201 op_sel_hi:[0,0,0]
	v_mfma_scale_f32_16x16x128_f8f6f4 v[90:93], v[10:17], v[204:211], v[90:93], v201, v201 op_sel_hi:[0,0,0]
	v_mfma_scale_f32_16x16x128_f8f6f4 v[78:81], v[2:9], v[212:219], v[78:81], v201, v201 op_sel_hi:[0,0,0]
	v_mfma_scale_f32_16x16x128_f8f6f4 v[74:77], v[10:17], v[212:219], v[74:77], v201, v201 op_sel_hi:[0,0,0]
	v_mfma_scale_f32_16x16x128_f8f6f4 v[62:65], v[2:9], v[220:227], v[62:65], v201, v201 op_sel_hi:[0,0,0]
	v_mfma_scale_f32_16x16x128_f8f6f4 v[58:61], v[10:17], v[220:227], v[58:61], v201, v201 op_sel_hi:[0,0,0]
	v_mfma_scale_f32_16x16x128_f8f6f4 v[46:49], v[2:9], v[228:235], v[46:49], v201, v201 op_sel_hi:[0,0,0]
	v_mfma_scale_f32_16x16x128_f8f6f4 v[42:45], v[10:17], v[228:235], v[42:45], v201, v201 op_sel_hi:[0,0,0]
	s_setprio 0
	s_setprio 1
	v_mfma_scale_f32_16x16x128_f8f6f4 v[86:89], v[18:25], v[204:211], v[86:89], v201, v201 op_sel_hi:[0,0,0]
	v_mfma_scale_f32_16x16x128_f8f6f4 v[82:85], v[26:33], v[204:211], v[82:85], v201, v201 op_sel_hi:[0,0,0]
	v_mfma_scale_f32_16x16x128_f8f6f4 v[70:73], v[18:25], v[212:219], v[70:73], v201, v201 op_sel_hi:[0,0,0]
	v_mfma_scale_f32_16x16x128_f8f6f4 v[66:69], v[26:33], v[212:219], v[66:69], v201, v201 op_sel_hi:[0,0,0]
	v_mfma_scale_f32_16x16x128_f8f6f4 v[54:57], v[18:25], v[220:227], v[54:57], v201, v201 op_sel_hi:[0,0,0]
	v_mfma_scale_f32_16x16x128_f8f6f4 v[50:53], v[26:33], v[220:227], v[50:53], v201, v201 op_sel_hi:[0,0,0]
	v_mfma_scale_f32_16x16x128_f8f6f4 v[38:41], v[18:25], v[228:235], v[38:41], v201, v201 op_sel_hi:[0,0,0]
	v_mfma_scale_f32_16x16x128_f8f6f4 v[34:37], v[26:33], v[228:235], v[34:37], v201, v201 op_sel_hi:[0,0,0]
	s_setprio 0
	s_barrier
	s_add_i32 s64, s64, 2
	s_add_u32 s80, s80, 0x100
	s_addc_u32 s81, s81, 0
	s_add_u32 s52, s52, 0x100
	s_addc_u32 s53, s53, 0
	s_cmp_gt_u32 s64, 13
	s_cbranch_scc0 .LBB0_123
	s_nop 15
	s_nop 7
	s_and_b64 vcc, exec, s[60:61]
	s_cbranch_vccz .LBB0_126
	s_barrier

;     __device__ __forceinline__ void operator()(const f32x4 (&acc)[2][2][4][2], const Unit& u, int wr, int wc, int fr, int fq) const {
;         const int row0 = u.pm * BM + wr * 64 + fr; const int col0 = u.pn * BM + wc * 32 + 4 * fq; const float* gb = g1 + (size_t)(u.pm / tiles_per_batch) * g1_stride;
;         f32x4 gv[2][2];
; #pragma unroll
;         for (int bj = 0; bj < 2; ++bj)
; #pragma unroll
;             for (int n = 0; n < 2; ++n) gv[bj][n] = *(const f32x4*)(gb + col0 + bj * HALF + n * 16);
; #pragma unroll
;         for (int ai = 0; ai < 2; ++ai)
; #pragma unroll
;             for (int m = 0; m < 4; ++m) { const size_t off = (size_t)(row0 + ai * HALF + m * 16) * 2048 + col0;
; #pragma unroll
;                 for (int bj = 0; bj < 2; ++bj)
; #pragma unroll
;                     for (int n = 0; n < 2; ++n) { const f32x4 xv = *(const f32x4*)(X + off + bj * HALF + n * 16);
;                         *(f32x4*)(H1 + off + bj * HALF + n * 16) = xv + gv[bj][n] * (acc[ai][bj][m][n] * wscale); } }
.LBB0_828:
	s_ashr_i32 s47, s60, 31
	s_lshr_b32 s47, s47, 28
	v_lshl_add_u32 v26, s60, 8, v186
	v_lshl_or_b32 v20, s69, 8, v188
	s_add_i32 s47, s60, s47
	v_ashrrev_i32_e32 v27, 31, v26
	s_ashr_i32 s47, s47, 4
	v_ashrrev_i32_e32 v21, 31, v20
	v_lshlrev_b64 v[4:5], 11, v[26:27]
	s_mul_hi_i32 s55, s47, 0xc000
	s_mul_i32 s47, s47, 0xc000
	v_lshl_add_u64 v[4:5], v[4:5], 0, v[20:21]
	v_readlane_b32 s64, v246, 3
	s_add_u32 s62, s49, s47
	v_lshlrev_b64 v[18:19], 2, v[4:5]
	v_readlane_b32 s65, v246, 4
	s_addc_u32 s63, s50, s55
	v_lshl_add_u64 v[2:3], v[20:21], 2, s[62:63]
	global_load_dwordx4 v[14:17], v[2:3], off
	global_load_dwordx4 v[10:13], v[2:3], off offset:64
	global_load_dwordx4 v[6:9], v[2:3], off offset:512
	s_nop 0
	global_load_dwordx4 v[2:5], v[2:3], off offset:576
	v_lshl_add_u64 v[178:179], s[64:65], 0, v[18:19]
	v_lshl_add_u64 v[180:181], s[14:15], 0, v[18:19]
	s_mov_b64 s[82:83], 0x20000
	s_mov_b64 s[84:85], 0x40000
	s_mov_b64 s[88:89], 0x60000
	s_andn2_b64 vcc, exec, s[4:5]
	s_mov_b64 s[4:5], -1
	v_readlane_b32 s66, v246, 5
	v_readlane_b32 s67, v246, 6
	v_readlane_b32 s68, v246, 7
	v_readlane_b32 s69, v246, 8
	v_readlane_b32 s70, v246, 9
	v_readlane_b32 s71, v246, 10
	v_readlane_b32 s72, v246, 11
	v_readlane_b32 s73, v246, 12
	v_readlane_b32 s74, v246, 13
	v_readlane_b32 s75, v246, 14
	v_readlane_b32 s76, v246, 15
	v_readlane_b32 s77, v246, 16
	v_readlane_b32 s78, v246, 17
	v_readlane_b32 s79, v246, 18
	global_load_dwordx4 v[204:207], v[178:179], off
	global_load_dwordx4 v[208:211], v[178:179], off offset:64
	global_load_dwordx4 v[212:215], v[178:179], off offset:512
	global_load_dwordx4 v[216:219], v[178:179], off offset:576
	v_lshl_add_u64 v[236:237], v[178:179], 0, s[82:83]
	global_load_dwordx4 v[220:223], v[236:237], off
	global_load_dwordx4 v[224:227], v[236:237], off offset:64
	global_load_dwordx4 v[228:231], v[236:237], off offset:512
	global_load_dwordx4 v[232:235], v[236:237], off offset:576
	s_waitcnt vmcnt(7)
	v_pk_mul_f32 v[240:241], v[160:161], s[36:37] op_sel_hi:[1,0]
	v_pk_mul_f32 v[242:243], v[158:159], s[36:37] op_sel_hi:[1,0]
	v_pk_fma_f32 v[206:207], v[240:241], v[16:17], v[206:207]
	v_pk_fma_f32 v[204:205], v[242:243], v[14:15], v[204:205]
	global_store_dwordx4 v[180:181], v[204:207], off
	v_lshl_add_u64 v[236:237], v[178:179], 0, s[84:85]
	global_load_dwordx4 v[204:207], v[236:237], off
	s_waitcnt vmcnt(8)
	v_pk_mul_f32 v[240:241], v[156:157], s[36:37] op_sel_hi:[1,0]
	v_pk_mul_f32 v[242:243], v[154:155], s[36:37] op_sel_hi:[1,0]
	v_pk_fma_f32 v[210:211], v[240:241], v[12:13], v[210:211]
	v_pk_fma_f32 v[208:209], v[242:243], v[10:11], v[208:209]
	global_store_dwordx4 v[180:181], v[208:211], off offset:64
	global_load_dwordx4 v[208:211], v[236:237], off offset:64
	s_waitcnt vmcnt(9)
	v_pk_mul_f32 v[240:241], v[152:153], s[36:37] op_sel_hi:[1,0]
	v_pk_mul_f32 v[242:243], v[150:151], s[36:37] op_sel_hi:[1,0]
	v_pk_fma_f32 v[214:215], v[240:241], v[8:9], v[214:215]
	v_pk_fma_f32 v[212:213], v[242:243], v[6:7], v[212:213]
	global_store_dwordx4 v[180:181], v[212:215], off offset:512
	global_load_dwordx4 v[212:215], v[236:237], off offset:512
	s_waitcnt vmcnt(10)
	v_pk_mul_f32 v[240:241], v[144:145], s[36:37] op_sel_hi:[1,0]
	v_pk_mul_f32 v[242:243], v[142:143], s[36:37] op_sel_hi:[1,0]
	v_pk_fma_f32 v[218:219], v[240:241], v[4:5], v[218:219]
	v_pk_fma_f32 v[216:217], v[242:243], v[2:3], v[216:217]
	global_store_dwordx4 v[180:181], v[216:219], off offset:576
	global_load_dwordx4 v[216:219], v[236:237], off offset:576
	v_lshl_add_u64 v[238:239], v[180:181], 0, s[82:83]
	s_waitcnt vmcnt(11)
	v_pk_mul_f32 v[240:241], v[148:149], s[36:37] op_sel_hi:[1,0]
	v_pk_mul_f32 v[242:243], v[146:147], s[36:37] op_sel_hi:[1,0]
	v_pk_fma_f32 v[222:223], v[240:241], v[16:17], v[222:223]
	v_pk_fma_f32 v[220:221], v[242:243], v[14:15], v[220:221]
	global_store_dwordx4 v[238:239], v[220:223], off
	v_lshl_add_u64 v[236:237], v[178:179], 0, s[88:89]
	global_load_dwordx4 v[220:223], v[236:237], off
	s_waitcnt vmcnt(12)
	v_pk_mul_f32 v[240:241], v[140:141], s[36:37] op_sel_hi:[1,0]
	v_pk_mul_f32 v[242:243], v[138:139], s[36:37] op_sel_hi:[1,0]
	v_pk_fma_f32 v[226:227], v[240:241], v[12:13], v[226:227]
	v_pk_fma_f32 v[224:225], v[242:243], v[10:11], v[224:225]
	global_store_dwordx4 v[238:239], v[224:227], off offset:64
	global_load_dwordx4 v[224:227], v[236:237], off offset:64
	s_waitcnt vmcnt(13)
	v_pk_mul_f32 v[240:241], v[136:137], s[36:37] op_sel_hi:[1,0]
	v_pk_mul_f32 v[242:243], v[134:135], s[36:37] op_sel_hi:[1,0]
	v_pk_fma_f32 v[230:231], v[240:241], v[8:9], v[230:231]
	v_pk_fma_f32 v[228:229], v[242:243], v[6:7], v[228:229]
	global_store_dwordx4 v[238:239], v[228:231], off offset:512
	global_load_dwordx4 v[228:231], v[236:237], off offset:512
	s_waitcnt vmcnt(14)
	v_pk_mul_f32 v[240:241], v[128:129], s[36:37] op_sel_hi:[1,0]
	v_pk_mul_f32 v[242:243], v[126:127], s[36:37] op_sel_hi:[1,0]
	v_pk_fma_f32 v[234:235], v[240:241], v[4:5], v[234:235]
	v_pk_fma_f32 v[232:233], v[242:243], v[2:3], v[232:233]
	global_store_dwordx4 v[238:239], v[232:235], off offset:576
	global_load_dwordx4 v[232:235], v[236:237], off offset:576
	v_lshl_add_u64 v[238:239], v[180:181], 0, s[84:85]
	s_waitcnt vmcnt(14)
	v_pk_mul_f32 v[240:241], v[132:133], s[36:37] op_sel_hi:[1,0]
	v_pk_mul_f32 v[242:243], v[130:131], s[36:37] op_sel_hi:[1,0]
	v_pk_fma_f32 v[206:207], v[240:241], v[16:17], v[206:207]
	v_pk_fma_f32 v[204:205], v[242:243], v[14:15], v[204:205]
	global_store_dwordx4 v[238:239], v[204:207], off
	v_lshl_add_u64 v[236:237], v[178:179], 0, s[38:39]
	global_load_dwordx4 v[204:207], v[236:237], off
	s_waitcnt vmcnt(14)
;     __device__ __forceinline__ void operator()(const f32x4 (&acc)[2][2][4][2], const Unit& u, int wr, int wc, int fr, int fq) const {
;     ...
; #pragma unroll
;         for (int ai = 0; ai < 2; ++ai)
; #pragma unroll
;             for (int m = 0; m < 4; ++m) { const size_t off = (size_t)(row0 + ai * HALF + m * 16) * 2048 + col0;
; #pragma unroll
;                 for (int bj = 0; bj < 2; ++bj)
; #pragma unroll
;                     for (int n = 0; n < 2; ++n) { const f32x4 xv = *(const f32x4*)(X + off + bj * HALF + n * 16);
;                         *(f32x4*)(H1 + off + bj * HALF + n * 16) = xv + gv[bj][n] * (acc[ai][bj][m][n] * wscale); } }
	v_pk_mul_f32 v[240:241], v[124:125], s[36:37] op_sel_hi:[1,0]
	v_pk_mul_f32 v[242:243], v[122:123], s[36:37] op_sel_hi:[1,0]
	v_pk_fma_f32 v[210:211], v[240:241], v[12:13], v[210:211]
	v_pk_fma_f32 v[208:209], v[242:243], v[10:11], v[208:209]
	global_store_dwordx4 v[238:239], v[208:211], off offset:64
	global_load_dwordx4 v[208:211], v[236:237], off offset:64
	s_waitcnt vmcnt(14)
	v_pk_mul_f32 v[240:241], v[120:121], s[36:37] op_sel_hi:[1,0]
	v_pk_mul_f32 v[242:243], v[118:119], s[36:37] op_sel_hi:[1,0]
	v_pk_fma_f32 v[214:215], v[240:241], v[8:9], v[214:215]
	v_pk_fma_f32 v[212:213], v[242:243], v[6:7], v[212:213]
	global_store_dwordx4 v[238:239], v[212:215], off offset:512
	global_load_dwordx4 v[212:215], v[236:237], off offset:512
	s_waitcnt vmcnt(14)
	v_pk_mul_f32 v[240:241], v[112:113], s[36:37] op_sel_hi:[1,0]
	v_pk_mul_f32 v[242:243], v[110:111], s[36:37] op_sel_hi:[1,0]
	v_pk_fma_f32 v[218:219], v[240:241], v[4:5], v[218:219]
	v_pk_fma_f32 v[216:217], v[242:243], v[2:3], v[216:217]
	global_store_dwordx4 v[238:239], v[216:219], off offset:576
	global_load_dwordx4 v[216:219], v[236:237], off offset:576
	v_lshl_add_u64 v[238:239], v[180:181], 0, s[88:89]
	s_waitcnt vmcnt(14)
	v_pk_mul_f32 v[240:241], v[116:117], s[36:37] op_sel_hi:[1,0]
	v_pk_mul_f32 v[242:243], v[114:115], s[36:37] op_sel_hi:[1,0]
	v_pk_fma_f32 v[222:223], v[240:241], v[16:17], v[222:223]
	v_pk_fma_f32 v[220:221], v[242:243], v[14:15], v[220:221]
	global_store_dwordx4 v[238:239], v[220:223], off
	v_lshl_add_u64 v[236:237], v[178:179], 0, s[40:41]
	global_load_dwordx4 v[220:223], v[236:237], off
	s_waitcnt vmcnt(14)
	v_pk_mul_f32 v[240:241], v[108:109], s[36:37] op_sel_hi:[1,0]
	v_pk_mul_f32 v[242:243], v[106:107], s[36:37] op_sel_hi:[1,0]
	v_pk_fma_f32 v[226:227], v[240:241], v[12:13], v[226:227]
	v_pk_fma_f32 v[224:225], v[242:243], v[10:11], v[224:225]
	global_store_dwordx4 v[238:239], v[224:227], off offset:64
	global_load_dwordx4 v[224:227], v[236:237], off offset:64
	s_waitcnt vmcnt(14)
	v_pk_mul_f32 v[240:241], v[104:105], s[36:37] op_sel_hi:[1,0]
	v_pk_mul_f32 v[242:243], v[102:103], s[36:37] op_sel_hi:[1,0]
	v_pk_fma_f32 v[230:231], v[240:241], v[8:9], v[230:231]
	v_pk_fma_f32 v[228:229], v[242:243], v[6:7], v[228:229]
	global_store_dwordx4 v[238:239], v[228:231], off offset:512
	global_load_dwordx4 v[228:231], v[236:237], off offset:512
	s_waitcnt vmcnt(14)
	v_pk_mul_f32 v[240:241], v[100:101], s[36:37] op_sel_hi:[1,0]
	v_pk_mul_f32 v[242:243], v[98:99], s[36:37] op_sel_hi:[1,0]
	v_pk_fma_f32 v[234:235], v[240:241], v[4:5], v[234:235]
	v_pk_fma_f32 v[232:233], v[242:243], v[2:3], v[232:233]
	global_store_dwordx4 v[238:239], v[232:235], off offset:576
	global_load_dwordx4 v[232:235], v[236:237], off offset:576
	v_lshl_add_u64 v[238:239], v[180:181], 0, s[38:39]
	s_waitcnt vmcnt(14)
	v_pk_mul_f32 v[240:241], v[96:97], s[36:37] op_sel_hi:[1,0]
	v_pk_mul_f32 v[242:243], v[94:95], s[36:37] op_sel_hi:[1,0]
	v_pk_fma_f32 v[206:207], v[240:241], v[16:17], v[206:207]
	v_pk_fma_f32 v[204:205], v[242:243], v[14:15], v[204:205]
	global_store_dwordx4 v[238:239], v[204:207], off
	v_lshl_add_u64 v[236:237], v[178:179], 0, s[42:43]
	global_load_dwordx4 v[204:207], v[236:237], off
	s_waitcnt vmcnt(14)
	v_pk_mul_f32 v[240:241], v[92:93], s[36:37] op_sel_hi:[1,0]
	v_pk_mul_f32 v[242:243], v[90:91], s[36:37] op_sel_hi:[1,0]
	v_pk_fma_f32 v[210:211], v[240:241], v[12:13], v[210:211]
	v_pk_fma_f32 v[208:209], v[242:243], v[10:11], v[208:209]
	global_store_dwordx4 v[238:239], v[208:211], off offset:64
	global_load_dwordx4 v[208:211], v[236:237], off offset:64
	s_waitcnt vmcnt(14)
	v_pk_mul_f32 v[240:241], v[88:89], s[36:37] op_sel_hi:[1,0]
	v_pk_mul_f32 v[242:243], v[86:87], s[36:37] op_sel_hi:[1,0]
	v_pk_fma_f32 v[214:215], v[240:241], v[8:9], v[214:215]
	v_pk_fma_f32 v[212:213], v[242:243], v[6:7], v[212:213]
	global_store_dwordx4 v[238:239], v[212:215], off offset:512
	global_load_dwordx4 v[212:215], v[236:237], off offset:512
	s_waitcnt vmcnt(14)
	v_pk_mul_f32 v[240:241], v[80:81], s[36:37] op_sel_hi:[1,0]
	v_pk_mul_f32 v[242:243], v[78:79], s[36:37] op_sel_hi:[1,0]
	v_pk_fma_f32 v[218:219], v[240:241], v[4:5], v[218:219]
	v_pk_fma_f32 v[216:217], v[242:243], v[2:3], v[216:217]
	global_store_dwordx4 v[238:239], v[216:219], off offset:576
	global_load_dwordx4 v[216:219], v[236:237], off offset:576
	v_lshl_add_u64 v[238:239], v[180:181], 0, s[40:41]
	s_waitcnt vmcnt(14)
;     __device__ __forceinline__ void operator()(const f32x4 (&acc)[2][2][4][2], const Unit& u, int wr, int wc, int fr, int fq) const {
;     ...
; #pragma unroll
;         for (int ai = 0; ai < 2; ++ai)
; #pragma unroll
;             for (int m = 0; m < 4; ++m) { const size_t off = (size_t)(row0 + ai * HALF + m * 16) * 2048 + col0;
; #pragma unroll
;                 for (int bj = 0; bj < 2; ++bj)
; #pragma unroll
;                     for (int n = 0; n < 2; ++n) { const f32x4 xv = *(const f32x4*)(X + off + bj * HALF + n * 16);
;                         *(f32x4*)(H1 + off + bj * HALF + n * 16) = xv + gv[bj][n] * (acc[ai][bj][m][n] * wscale); } }
	v_pk_mul_f32 v[240:241], v[84:85], s[36:37] op_sel_hi:[1,0]
	v_pk_mul_f32 v[242:243], v[82:83], s[36:37] op_sel_hi:[1,0]
	v_pk_fma_f32 v[222:223], v[240:241], v[16:17], v[222:223]
	v_pk_fma_f32 v[220:221], v[242:243], v[14:15], v[220:221]
	global_store_dwordx4 v[238:239], v[220:223], off
	v_lshl_add_u64 v[236:237], v[178:179], 0, s[44:45]
	global_load_dwordx4 v[220:223], v[236:237], off
	s_waitcnt vmcnt(14)
	v_pk_mul_f32 v[240:241], v[76:77], s[36:37] op_sel_hi:[1,0]
	v_pk_mul_f32 v[242:243], v[74:75], s[36:37] op_sel_hi:[1,0]
	v_pk_fma_f32 v[226:227], v[240:241], v[12:13], v[226:227]
	v_pk_fma_f32 v[224:225], v[242:243], v[10:11], v[224:225]
	global_store_dwordx4 v[238:239], v[224:227], off offset:64
	global_load_dwordx4 v[224:227], v[236:237], off offset:64
	s_waitcnt vmcnt(14)
	v_pk_mul_f32 v[240:241], v[72:73], s[36:37] op_sel_hi:[1,0]
	v_pk_mul_f32 v[242:243], v[70:71], s[36:37] op_sel_hi:[1,0]
	v_pk_fma_f32 v[230:231], v[240:241], v[8:9], v[230:231]
	v_pk_fma_f32 v[228:229], v[242:243], v[6:7], v[228:229]
	global_store_dwordx4 v[238:239], v[228:231], off offset:512
	global_load_dwordx4 v[228:231], v[236:237], off offset:512
	s_waitcnt vmcnt(14)
	v_pk_mul_f32 v[240:241], v[64:65], s[36:37] op_sel_hi:[1,0]
	v_pk_mul_f32 v[242:243], v[62:63], s[36:37] op_sel_hi:[1,0]
	v_pk_fma_f32 v[234:235], v[240:241], v[4:5], v[234:235]
	v_pk_fma_f32 v[232:233], v[242:243], v[2:3], v[232:233]
	global_store_dwordx4 v[238:239], v[232:235], off offset:576
	global_load_dwordx4 v[232:235], v[236:237], off offset:576
	v_lshl_add_u64 v[238:239], v[180:181], 0, s[42:43]
	s_waitcnt vmcnt(14)
	v_pk_mul_f32 v[240:241], v[68:69], s[36:37] op_sel_hi:[1,0]
	v_pk_mul_f32 v[242:243], v[66:67], s[36:37] op_sel_hi:[1,0]
	v_pk_fma_f32 v[206:207], v[240:241], v[16:17], v[206:207]
	v_pk_fma_f32 v[204:205], v[242:243], v[14:15], v[204:205]
	global_store_dwordx4 v[238:239], v[204:207], off
	s_waitcnt vmcnt(13)
	v_pk_mul_f32 v[240:241], v[60:61], s[36:37] op_sel_hi:[1,0]
	v_pk_mul_f32 v[242:243], v[58:59], s[36:37] op_sel_hi:[1,0]
	v_pk_fma_f32 v[210:211], v[240:241], v[12:13], v[210:211]
	v_pk_fma_f32 v[208:209], v[242:243], v[10:11], v[208:209]
	global_store_dwordx4 v[238:239], v[208:211], off offset:64
	s_waitcnt vmcnt(12)
	v_pk_mul_f32 v[240:241], v[56:57], s[36:37] op_sel_hi:[1,0]
	v_pk_mul_f32 v[242:243], v[54:55], s[36:37] op_sel_hi:[1,0]
	v_pk_fma_f32 v[214:215], v[240:241], v[8:9], v[214:215]
	v_pk_fma_f32 v[212:213], v[242:243], v[6:7], v[212:213]
	global_store_dwordx4 v[238:239], v[212:215], off offset:512
	s_waitcnt vmcnt(11)
	v_pk_mul_f32 v[240:241], v[48:49], s[36:37] op_sel_hi:[1,0]
	v_pk_mul_f32 v[242:243], v[46:47], s[36:37] op_sel_hi:[1,0]
	v_pk_fma_f32 v[218:219], v[240:241], v[4:5], v[218:219]
	v_pk_fma_f32 v[216:217], v[242:243], v[2:3], v[216:217]
	global_store_dwordx4 v[238:239], v[216:219], off offset:576
	v_lshl_add_u64 v[238:239], v[180:181], 0, s[44:45]
	s_waitcnt vmcnt(10)
	v_pk_mul_f32 v[240:241], v[52:53], s[36:37] op_sel_hi:[1,0]
	v_pk_mul_f32 v[242:243], v[50:51], s[36:37] op_sel_hi:[1,0]
	v_pk_fma_f32 v[222:223], v[240:241], v[16:17], v[222:223]
	v_pk_fma_f32 v[220:221], v[242:243], v[14:15], v[220:221]
	global_store_dwordx4 v[238:239], v[220:223], off
	s_waitcnt vmcnt(9)
	v_pk_mul_f32 v[240:241], v[44:45], s[36:37] op_sel_hi:[1,0]
	v_pk_mul_f32 v[242:243], v[42:43], s[36:37] op_sel_hi:[1,0]
	v_pk_fma_f32 v[226:227], v[240:241], v[12:13], v[226:227]
	v_pk_fma_f32 v[224:225], v[242:243], v[10:11], v[224:225]
	global_store_dwordx4 v[238:239], v[224:227], off offset:64
	s_waitcnt vmcnt(8)
	v_pk_mul_f32 v[240:241], v[40:41], s[36:37] op_sel_hi:[1,0]
	v_pk_mul_f32 v[242:243], v[38:39], s[36:37] op_sel_hi:[1,0]
	v_pk_fma_f32 v[230:231], v[240:241], v[8:9], v[230:231]
	v_pk_fma_f32 v[228:229], v[242:243], v[6:7], v[228:229]
	global_store_dwordx4 v[238:239], v[228:231], off offset:512
	s_waitcnt vmcnt(7)
	v_pk_mul_f32 v[240:241], v[36:37], s[36:37] op_sel_hi:[1,0]
	v_pk_mul_f32 v[242:243], v[34:35], s[36:37] op_sel_hi:[1,0]
	v_pk_fma_f32 v[234:235], v[240:241], v[4:5], v[234:235]
	v_pk_fma_f32 v[232:233], v[242:243], v[2:3], v[232:233]
	global_store_dwordx4 v[238:239], v[232:235], off offset:576
	s_cbranch_vccnz .LBB0_817
	s_andn2_b64 vcc, exec, s[8:9]
	s_cbranch_vccnz .LBB0_816
	s_barrier
	s_branch .LBB0_816

; #define PG8_STAGE(bufoff, gbase, voff) do { _Pragma("unroll") for (int _i = 0; _i < 2; ++_i) \
;         __builtin_amdgcn_global_load_lds((const unsigned*)((const char*)(gbase) + (voff)[_i]), (PG8_LAS unsigned*)(lds + (bufoff) + ldsw + _i * 8192), 16, 0, 0); } while (0)
; #define PG8_LDA(dst, b, h) do { _Pragma("unroll") for (int m = 0; m < 4; ++m) _Pragma("unroll") for (int k = 0; k < 2; ++k) dst[m][k] = *(const PG8_LAS bf16x8*)(lds + PG8_SA(b, h) + aoff + m * 2048 + k * 1024); } while (0)
; #define PG8_LDB(dst, b, h) do { _Pragma("unroll") for (int n = 0; n < 2; ++n) _Pragma("unroll") for (int k = 0; k < 2; ++k) dst[n][k] = *(const PG8_LAS bf16x8*)(lds + PG8_SB(b, h) + boff + n * 2048 + k * 1024); } while (0)
; #define PG8_WAIT_V(n) asm volatile("s_waitcnt vmcnt(" #n ")" ::: "memory")
; #define PG8_WAIT_L(n) asm volatile("s_waitcnt lgkmcnt(" #n ")" ::: "memory")
; #define PG8_BAR __builtin_amdgcn_s_barrier()
; #define PG8_SCHED __builtin_amdgcn_sched_barrier(0)
; template <class Epi, class Sched, bool ALIGN_EPI = false, bool SP2 = false, bool F8 = false, bool GATHER = false>
; __device__ __forceinline__ void gemm_phase(PG8_LAS unsigned char* lds, const Gemm g, const Sched& S, const Epi& E) {
;     ...
;             PG8_LDB(B0, 0, 0); PG8_LDB(B1, 0, 1); PG8_SCHED; PG8_LDA(At, 0, 0); PG8_STAGE(PG8_SA(1, 1), a1, vo[1]);
;             PG8_WAIT_V(8); PG8_WAIT_L(0); PG8_BAR; PG8_MMA(0, 0, At, B0); PG8_MMA(0, 1, At, B1); PG8_BAR; PG8_SCHED;
;             PG8_LDA(At, 0, 1); PG8_STAGE(PG8_SB(0, 0), b2, voffB); PG8_STAGE(PG8_SB(0, 1), b2 + hstep, voffB); PG8_STAGE(PG8_SA(0, 0), a2, s0);
;             PG8_WAIT_V(8); PG8_WAIT_L(0); PG8_BAR; PG8_MMA(1, 0, At, B0); PG8_MMA(1, 1, At, B1); PG8_BAR; PG8_SCHED;
.LBB0_996:
	ds_read_b128 v[26:29], v196
	ds_read_b128 v[30:33], v196 offset:1024
	ds_read_b128 v[18:21], v196 offset:2048
	ds_read_b128 v[22:25], v196 offset:3072
	ds_read_b128 v[10:13], v197
	ds_read_b128 v[14:17], v197 offset:1024
	ds_read_b128 v[2:5], v197 offset:2048
	ds_read_b128 v[6:9], v197 offset:3072
	s_add_u32 s50, s30, s48
	s_addc_u32 s51, s31, s49
	s_add_u32 s52, s50, 0x4000100
	s_addc_u32 s53, s51, 0
	s_add_u32 s67, s64, s48
	s_addc_u32 s68, s65, s49
	s_cmpk_eq_i32 s48, 0x700
	s_cselect_b64 vcc, -1, 0
	s_and_b64 s[50:51], vcc, exec
	v_cndmask_b32_e32 v162, v205, v204, vcc
	s_cselect_b32 s53, s15, s53
	s_cselect_b32 s52, s14, s52
	v_cndmask_b32_e32 v169, v168, v201, vcc
	v_cndmask_b32_e32 v238, v170, v203, vcc
	v_cndmask_b32_e32 v173, v172, v202, vcc
	s_cselect_b32 s51, s43, s68
	s_cselect_b32 s50, s63, s67
	v_lshl_add_u64 v[230:231], v[176:177], 0, s[48:49]
	s_add_i32 m0, s9, 0xc000
	ds_read_b128 v[178:181], v198
	ds_read_b128 v[182:185], v198 offset:1024
	ds_read_b128 v[206:209], v198 offset:2048
	ds_read_b128 v[210:213], v198 offset:3072
	ds_read_b128 v[214:217], v198 offset:4096
	ds_read_b128 v[218:221], v198 offset:5120
	ds_read_b128 v[222:225], v198 offset:6144
	ds_read_b128 v[226:229], v198 offset:7168
	global_load_lds_dwordx4 v[230:231], off
	v_lshl_add_u64 v[230:231], v[174:175], 0, s[48:49]
	s_add_i32 m0, s9, 0xe000
	s_nop 0
	global_load_lds_dwordx4 v[230:231], off
	s_waitcnt vmcnt(8)
	s_waitcnt lgkmcnt(0)
	s_barrier
	s_setprio 1
	s_waitcnt lgkmcnt(0)
	v_mfma_scale_f32_16x16x128_f8f6f4 v[158:161], v[26:33], v[178:185], v[158:161], v199, v199 op_sel_hi:[0,0,0]
	v_mfma_scale_f32_16x16x128_f8f6f4 v[154:157], v[18:25], v[178:185], v[154:157], v199, v199 op_sel_hi:[0,0,0]
	v_mfma_scale_f32_16x16x128_f8f6f4 v[142:145], v[26:33], v[206:213], v[142:145], v199, v199 op_sel_hi:[0,0,0]
	v_mfma_scale_f32_16x16x128_f8f6f4 v[134:137], v[18:25], v[206:213], v[134:137], v199, v199 op_sel_hi:[0,0,0]
	v_mfma_scale_f32_16x16x128_f8f6f4 v[126:129], v[26:33], v[214:221], v[126:129], v199, v199 op_sel_hi:[0,0,0]
	v_mfma_scale_f32_16x16x128_f8f6f4 v[118:121], v[18:25], v[214:221], v[118:121], v199, v199 op_sel_hi:[0,0,0]
	v_mfma_scale_f32_16x16x128_f8f6f4 v[110:113], v[26:33], v[222:229], v[110:113], v199, v199 op_sel_hi:[0,0,0]
	v_mfma_scale_f32_16x16x128_f8f6f4 v[102:105], v[18:25], v[222:229], v[102:105], v199, v199 op_sel_hi:[0,0,0]
	s_setprio 0
	s_setprio 1
	v_mfma_scale_f32_16x16x128_f8f6f4 v[150:153], v[10:17], v[178:185], v[150:153], v199, v199 op_sel_hi:[0,0,0]
	v_mfma_scale_f32_16x16x128_f8f6f4 v[146:149], v[2:9], v[178:185], v[146:149], v199, v199 op_sel_hi:[0,0,0]
	v_mfma_scale_f32_16x16x128_f8f6f4 v[138:141], v[10:17], v[206:213], v[138:141], v199, v199 op_sel_hi:[0,0,0]
	v_mfma_scale_f32_16x16x128_f8f6f4 v[130:133], v[2:9], v[206:213], v[130:133], v199, v199 op_sel_hi:[0,0,0]
	v_mfma_scale_f32_16x16x128_f8f6f4 v[122:125], v[10:17], v[214:221], v[122:125], v199, v199 op_sel_hi:[0,0,0]
	v_mfma_scale_f32_16x16x128_f8f6f4 v[114:117], v[2:9], v[214:221], v[114:117], v199, v199 op_sel_hi:[0,0,0]
	v_mfma_scale_f32_16x16x128_f8f6f4 v[106:109], v[10:17], v[222:229], v[106:109], v199, v199 op_sel_hi:[0,0,0]
	v_mfma_scale_f32_16x16x128_f8f6f4 v[98:101], v[2:9], v[222:229], v[98:101], v199, v199 op_sel_hi:[0,0,0]
	s_setprio 0
	s_barrier
	s_add_i32 s67, s55, s1
	v_lshl_add_u64 v[178:179], s[50:51], 0, v[164:165]
	s_mov_b32 m0, s67
	ds_read_b128 v[206:209], v198 offset:16384
	ds_read_b128 v[210:213], v198 offset:17408
	ds_read_b128 v[214:217], v198 offset:18432
	ds_read_b128 v[218:221], v198 offset:19456
	ds_read_b128 v[222:225], v198 offset:20480
	ds_read_b128 v[226:229], v198 offset:21504
	ds_read_b128 v[230:233], v198 offset:22528
	ds_read_b128 v[234:237], v198 offset:23552
	global_load_lds_dwordx4 v[178:179], off
	s_add_i32 m0, s67, 0x2000
	s_add_u32 s68, s50, 0x40000
	v_lshl_add_u64 v[180:181], s[50:51], 0, v[166:167]
	s_addc_u32 s69, s51, 0
	s_add_i32 s67, s56, s1
	global_load_lds_dwordx4 v[180:181], off
	v_lshl_add_u64 v[182:183], s[68:69], 0, v[164:165]
	s_mov_b32 m0, s67
	v_mov_b32_e32 v239, v163
	global_load_lds_dwordx4 v[182:183], off
	v_lshl_add_u64 v[182:183], s[68:69], 0, v[166:167]
	s_add_i32 m0, s67, 0x2000
	v_lshl_add_u64 v[184:185], s[52:53], 0, v[162:163]
	global_load_lds_dwordx4 v[182:183], off
	s_mov_b32 m0, s9
	v_lshl_add_u64 v[182:183], s[52:53], 0, v[238:239]
	global_load_lds_dwordx4 v162, s[52:53]
	s_mov_b32 m0, s10
	s_nop 0
	global_load_lds_dwordx4 v238, s[52:53]
	s_waitcnt vmcnt(8)
	s_waitcnt lgkmcnt(0)
	s_barrier
	s_setprio 1
	s_waitcnt lgkmcnt(0)
	v_mfma_scale_f32_16x16x128_f8f6f4 v[94:97], v[26:33], v[206:213], v[94:97], v199, v199 op_sel_hi:[0,0,0]
	v_mfma_scale_f32_16x16x128_f8f6f4 v[86:89], v[18:25], v[206:213], v[86:89], v199, v199 op_sel_hi:[0,0,0]
	v_mfma_scale_f32_16x16x128_f8f6f4 v[78:81], v[26:33], v[214:221], v[78:81], v199, v199 op_sel_hi:[0,0,0]
	v_mfma_scale_f32_16x16x128_f8f6f4 v[70:73], v[18:25], v[214:221], v[70:73], v199, v199 op_sel_hi:[0,0,0]
	v_mfma_scale_f32_16x16x128_f8f6f4 v[62:65], v[26:33], v[222:229], v[62:65], v199, v199 op_sel_hi:[0,0,0]
	v_mfma_scale_f32_16x16x128_f8f6f4 v[54:57], v[18:25], v[222:229], v[54:57], v199, v199 op_sel_hi:[0,0,0]
	v_mfma_scale_f32_16x16x128_f8f6f4 v[46:49], v[26:33], v[230:237], v[46:49], v199, v199 op_sel_hi:[0,0,0]
	v_mfma_scale_f32_16x16x128_f8f6f4 v[38:41], v[18:25], v[230:237], v[38:41], v199, v199 op_sel_hi:[0,0,0]
	s_setprio 0
	s_setprio 1
	v_mfma_scale_f32_16x16x128_f8f6f4 v[90:93], v[10:17], v[206:213], v[90:93], v199, v199 op_sel_hi:[0,0,0]
	v_mfma_scale_f32_16x16x128_f8f6f4 v[82:85], v[2:9], v[206:213], v[82:85], v199, v199 op_sel_hi:[0,0,0]
	v_mfma_scale_f32_16x16x128_f8f6f4 v[74:77], v[10:17], v[214:221], v[74:77], v199, v199 op_sel_hi:[0,0,0]
	v_mfma_scale_f32_16x16x128_f8f6f4 v[66:69], v[2:9], v[214:221], v[66:69], v199, v199 op_sel_hi:[0,0,0]
	v_mfma_scale_f32_16x16x128_f8f6f4 v[58:61], v[10:17], v[222:229], v[58:61], v199, v199 op_sel_hi:[0,0,0]
	v_mfma_scale_f32_16x16x128_f8f6f4 v[50:53], v[2:9], v[222:229], v[50:53], v199, v199 op_sel_hi:[0,0,0]
	v_mfma_scale_f32_16x16x128_f8f6f4 v[42:45], v[10:17], v[230:237], v[42:45], v199, v199 op_sel_hi:[0,0,0]
	v_mfma_scale_f32_16x16x128_f8f6f4 v[34:37], v[2:9], v[230:237], v[34:37], v199, v199 op_sel_hi:[0,0,0]
	s_setprio 0
	s_barrier
; #define PG8_STAGE(bufoff, gbase, voff) do { _Pragma("unroll") for (int _i = 0; _i < 2; ++_i) \
;         __builtin_amdgcn_global_load_lds((const unsigned*)((const char*)(gbase) + (voff)[_i]), (PG8_LAS unsigned*)(lds + (bufoff) + ldsw + _i * 8192), 16, 0, 0); } while (0)
; #define PG8_LDA(dst, b, h) do { _Pragma("unroll") for (int m = 0; m < 4; ++m) _Pragma("unroll") for (int k = 0; k < 2; ++k) dst[m][k] = *(const PG8_LAS bf16x8*)(lds + PG8_SA(b, h) + aoff + m * 2048 + k * 1024); } while (0)
; #define PG8_LDB(dst, b, h) do { _Pragma("unroll") for (int n = 0; n < 2; ++n) _Pragma("unroll") for (int k = 0; k < 2; ++k) dst[n][k] = *(const PG8_LAS bf16x8*)(lds + PG8_SB(b, h) + boff + n * 2048 + k * 1024); } while (0)
; #define PG8_WAIT_V(n) asm volatile("s_waitcnt vmcnt(" #n ")" ::: "memory")
; #define PG8_WAIT_L(n) asm volatile("s_waitcnt lgkmcnt(" #n ")" ::: "memory")
; #define PG8_BAR __builtin_amdgcn_s_barrier()
; #define PG8_SCHED __builtin_amdgcn_sched_barrier(0)
; template <class Epi, class Sched, bool ALIGN_EPI = false, bool SP2 = false, bool F8 = false, bool GATHER = false>
; __device__ __forceinline__ void gemm_phase(PG8_LAS unsigned char* lds, const Gemm g, const Sched& S, const Epi& E) {
;     ...
;             PG8_LDB(B0, 1, 0); PG8_LDB(B1, 1, 1); PG8_SCHED; PG8_LDA(At, 1, 0); PG8_STAGE(PG8_SA(0, 1), a2, s1);
;             PG8_WAIT_V(8); PG8_WAIT_L(0); PG8_BAR; PG8_MMA(0, 0, At, B0); PG8_MMA(0, 1, At, B1); PG8_BAR; PG8_SCHED;
;             PG8_LDA(At, 1, 1); PG8_STAGE(PG8_SB(1, 0), b3, voffB); PG8_STAGE(PG8_SB(1, 1), b3 + hstep, voffB); PG8_STAGE(PG8_SA(1, 0), a3, s0);
;             PG8_WAIT_V(8); PG8_WAIT_L(0); PG8_BAR; PG8_MMA(1, 0, At, B0); PG8_MMA(1, 1, At, B1); PG8_BAR; PG8_SCHED;
	s_add_i32 s67, 0, 0x18000
	s_add_i32 s68, 0, 0x1c000
	v_add_u32_e32 v14, s67, v194
	v_add_u32_e32 v30, s68, v194
	ds_read_b128 v[2:5], v14
	ds_read_b128 v[6:9], v14 offset:1024
	ds_read_b128 v[10:13], v14 offset:2048
	ds_read_b128 v[14:17], v14 offset:3072
	ds_read_b128 v[18:21], v30
	ds_read_b128 v[22:25], v30 offset:1024
	ds_read_b128 v[26:29], v30 offset:2048
	ds_read_b128 v[30:33], v30 offset:3072
	s_mov_b32 m0, s11
	ds_read_b128 v[206:209], v198 offset:32768
	ds_read_b128 v[210:213], v198 offset:33792
	ds_read_b128 v[214:217], v198 offset:34816
	ds_read_b128 v[218:221], v198 offset:35840
	ds_read_b128 v[222:225], v198 offset:36864
	ds_read_b128 v[226:229], v198 offset:37888
	ds_read_b128 v[230:233], v198 offset:38912
	ds_read_b128 v[234:237], v198 offset:39936
	global_load_lds_dwordx4 v169, s[52:53]
	s_mov_b32 m0, s33
	s_nop 0
	global_load_lds_dwordx4 v173, s[52:53]
	s_waitcnt vmcnt(8)
	s_waitcnt lgkmcnt(0)
	s_barrier
	s_setprio 1
	s_waitcnt lgkmcnt(0)
	v_mfma_scale_f32_16x16x128_f8f6f4 v[158:161], v[2:9], v[206:213], v[158:161], v199, v199 op_sel_hi:[0,0,0]
	v_mfma_scale_f32_16x16x128_f8f6f4 v[154:157], v[10:17], v[206:213], v[154:157], v199, v199 op_sel_hi:[0,0,0]
	v_mfma_scale_f32_16x16x128_f8f6f4 v[142:145], v[2:9], v[214:221], v[142:145], v199, v199 op_sel_hi:[0,0,0]
	v_mfma_scale_f32_16x16x128_f8f6f4 v[134:137], v[10:17], v[214:221], v[134:137], v199, v199 op_sel_hi:[0,0,0]
	v_mfma_scale_f32_16x16x128_f8f6f4 v[126:129], v[2:9], v[222:229], v[126:129], v199, v199 op_sel_hi:[0,0,0]
	v_mfma_scale_f32_16x16x128_f8f6f4 v[118:121], v[10:17], v[222:229], v[118:121], v199, v199 op_sel_hi:[0,0,0]
	v_mfma_scale_f32_16x16x128_f8f6f4 v[110:113], v[2:9], v[230:237], v[110:113], v199, v199 op_sel_hi:[0,0,0]
	v_mfma_scale_f32_16x16x128_f8f6f4 v[102:105], v[10:17], v[230:237], v[102:105], v199, v199 op_sel_hi:[0,0,0]
	s_setprio 0
	s_setprio 1
	v_mfma_scale_f32_16x16x128_f8f6f4 v[150:153], v[18:25], v[206:213], v[150:153], v199, v199 op_sel_hi:[0,0,0]
	v_mfma_scale_f32_16x16x128_f8f6f4 v[146:149], v[26:33], v[206:213], v[146:149], v199, v199 op_sel_hi:[0,0,0]
	v_mfma_scale_f32_16x16x128_f8f6f4 v[138:141], v[18:25], v[214:221], v[138:141], v199, v199 op_sel_hi:[0,0,0]
	v_mfma_scale_f32_16x16x128_f8f6f4 v[130:133], v[26:33], v[214:221], v[130:133], v199, v199 op_sel_hi:[0,0,0]
	v_mfma_scale_f32_16x16x128_f8f6f4 v[122:125], v[18:25], v[222:229], v[122:125], v199, v199 op_sel_hi:[0,0,0]
	v_mfma_scale_f32_16x16x128_f8f6f4 v[114:117], v[26:33], v[222:229], v[114:117], v199, v199 op_sel_hi:[0,0,0]
	v_mfma_scale_f32_16x16x128_f8f6f4 v[106:109], v[18:25], v[230:237], v[106:109], v199, v199 op_sel_hi:[0,0,0]
	v_mfma_scale_f32_16x16x128_f8f6f4 v[98:101], v[26:33], v[230:237], v[98:101], v199, v199 op_sel_hi:[0,0,0]
	s_setprio 0
	s_barrier
	s_add_i32 s52, s67, s1
	v_lshl_add_u64 v[178:179], v[178:179], 0, s[38:39]
	s_mov_b32 m0, s52
	ds_read_b128 v[206:209], v198 offset:49152
	ds_read_b128 v[210:213], v198 offset:50176
	ds_read_b128 v[214:217], v198 offset:51200
	ds_read_b128 v[218:221], v198 offset:52224
	ds_read_b128 v[222:225], v198 offset:53248
	ds_read_b128 v[226:229], v198 offset:54272
	ds_read_b128 v[230:233], v198 offset:55296
	ds_read_b128 v[234:237], v198 offset:56320
	global_load_lds_dwordx4 v[178:179], off
	s_add_i32 m0, s52, 0x2000
	s_add_u32 s50, s50, 0x40080
	v_lshl_add_u64 v[178:179], v[180:181], 0, s[38:39]
	s_addc_u32 s51, s51, 0
	s_add_i32 s52, s68, s1
	global_load_lds_dwordx4 v[178:179], off
	v_lshl_add_u64 v[178:179], s[50:51], 0, v[164:165]
	s_mov_b32 m0, s52
	s_nop 0
	global_load_lds_dwordx4 v[178:179], off
	v_lshl_add_u64 v[178:179], s[50:51], 0, v[166:167]
	s_add_i32 m0, s52, 0x2000
	s_nop 0
	global_load_lds_dwordx4 v[178:179], off
	v_lshl_add_u64 v[178:179], v[184:185], 0, s[38:39]
	s_mov_b32 m0, s47
	s_nop 0
	global_load_lds_dwordx4 v[178:179], off
	v_lshl_add_u64 v[178:179], v[182:183], 0, s[38:39]
	s_mov_b32 m0, s54
	s_nop 0
	global_load_lds_dwordx4 v[178:179], off
	s_waitcnt vmcnt(8)
	s_waitcnt lgkmcnt(0)
	s_barrier
	s_setprio 1
	s_waitcnt lgkmcnt(0)
	v_mfma_scale_f32_16x16x128_f8f6f4 v[94:97], v[2:9], v[206:213], v[94:97], v199, v199 op_sel_hi:[0,0,0]
	v_mfma_scale_f32_16x16x128_f8f6f4 v[86:89], v[10:17], v[206:213], v[86:89], v199, v199 op_sel_hi:[0,0,0]
	v_mfma_scale_f32_16x16x128_f8f6f4 v[78:81], v[2:9], v[214:221], v[78:81], v199, v199 op_sel_hi:[0,0,0]
	v_mfma_scale_f32_16x16x128_f8f6f4 v[70:73], v[10:17], v[214:221], v[70:73], v199, v199 op_sel_hi:[0,0,0]
	v_mfma_scale_f32_16x16x128_f8f6f4 v[62:65], v[2:9], v[222:229], v[62:65], v199, v199 op_sel_hi:[0,0,0]
	v_mfma_scale_f32_16x16x128_f8f6f4 v[54:57], v[10:17], v[222:229], v[54:57], v199, v199 op_sel_hi:[0,0,0]
	v_mfma_scale_f32_16x16x128_f8f6f4 v[46:49], v[2:9], v[230:237], v[46:49], v199, v199 op_sel_hi:[0,0,0]
	v_mfma_scale_f32_16x16x128_f8f6f4 v[38:41], v[10:17], v[230:237], v[38:41], v199, v199 op_sel_hi:[0,0,0]
	s_setprio 0
	s_setprio 1
	v_mfma_scale_f32_16x16x128_f8f6f4 v[90:93], v[18:25], v[206:213], v[90:93], v199, v199 op_sel_hi:[0,0,0]
	v_mfma_scale_f32_16x16x128_f8f6f4 v[82:85], v[26:33], v[206:213], v[82:85], v199, v199 op_sel_hi:[0,0,0]
	v_mfma_scale_f32_16x16x128_f8f6f4 v[74:77], v[18:25], v[214:221], v[74:77], v199, v199 op_sel_hi:[0,0,0]
	v_mfma_scale_f32_16x16x128_f8f6f4 v[66:69], v[26:33], v[214:221], v[66:69], v199, v199 op_sel_hi:[0,0,0]
	v_mfma_scale_f32_16x16x128_f8f6f4 v[58:61], v[18:25], v[222:229], v[58:61], v199, v199 op_sel_hi:[0,0,0]
	v_mfma_scale_f32_16x16x128_f8f6f4 v[50:53], v[26:33], v[222:229], v[50:53], v199, v199 op_sel_hi:[0,0,0]
	v_mfma_scale_f32_16x16x128_f8f6f4 v[42:45], v[18:25], v[230:237], v[42:45], v199, v199 op_sel_hi:[0,0,0]
	v_mfma_scale_f32_16x16x128_f8f6f4 v[34:37], v[26:33], v[230:237], v[34:37], v199, v199 op_sel_hi:[0,0,0]
	s_setprio 0
	s_barrier
	s_add_i32 s66, s66, 2
	s_add_u32 s48, s48, 0x100
	s_addc_u32 s49, s49, 0
	s_cmp_gt_u32 s66, 13
	s_cbranch_scc0 .LBB0_996
	s_nop 15
	s_nop 7
	s_and_b64 vcc, exec, s[40:41]
	s_cbranch_vccz .LBB0_999
	s_barrier

; #define PG8_STAGE(bufoff, gbase, voff) do { _Pragma("unroll") for (int _i = 0; _i < 2; ++_i) \
;         __builtin_amdgcn_global_load_lds((const unsigned*)((const char*)(gbase) + (voff)[_i]), (PG8_LAS unsigned*)(lds + (bufoff) + ldsw + _i * 8192), 16, 0, 0); } while (0)
; #define PG8_LDA(dst, b, h) do { _Pragma("unroll") for (int m = 0; m < 4; ++m) _Pragma("unroll") for (int k = 0; k < 2; ++k) dst[m][k] = *(const PG8_LAS bf16x8*)(lds + PG8_SA(b, h) + aoff + m * 2048 + k * 1024); } while (0)
; #define PG8_LDB(dst, b, h) do { _Pragma("unroll") for (int n = 0; n < 2; ++n) _Pragma("unroll") for (int k = 0; k < 2; ++k) dst[n][k] = *(const PG8_LAS bf16x8*)(lds + PG8_SB(b, h) + boff + n * 2048 + k * 1024); } while (0)
; #define PG8_WAIT_V(n) asm volatile("s_waitcnt vmcnt(" #n ")" ::: "memory")
; #define PG8_WAIT_L(n) asm volatile("s_waitcnt lgkmcnt(" #n ")" ::: "memory")
; #define PG8_BAR __builtin_amdgcn_s_barrier()
; #define PG8_SCHED __builtin_amdgcn_sched_barrier(0)
; template <class Epi, class Sched, bool ALIGN_EPI = false, bool SP2 = false, bool F8 = false, bool GATHER = false>
; __device__ __forceinline__ void gemm_phase(PG8_LAS unsigned char* lds, const Gemm g, const Sched& S, const Epi& E) {
;     ...
;             PG8_LDB(B0, 0, 0); PG8_LDB(B1, 0, 1); PG8_SCHED; PG8_LDA(At, 0, 0); PG8_STAGE(PG8_SA(1, 1), a1, vo[1]);
;             PG8_WAIT_V(8); PG8_WAIT_L(0); PG8_BAR; PG8_MMA(0, 0, At, B0); PG8_MMA(0, 1, At, B1); PG8_BAR; PG8_SCHED;
;             PG8_LDA(At, 0, 1); PG8_STAGE(PG8_SB(0, 0), b2, voffB); PG8_STAGE(PG8_SB(0, 1), b2 + hstep, voffB); PG8_STAGE(PG8_SA(0, 0), a2, s0);
;             PG8_WAIT_V(8); PG8_WAIT_L(0); PG8_BAR; PG8_MMA(1, 0, At, B0); PG8_MMA(1, 1, At, B1); PG8_BAR; PG8_SCHED;
.LBB0_1073:
	ds_read_b128 v[26:29], v196
	ds_read_b128 v[30:33], v196 offset:1024
	ds_read_b128 v[18:21], v196 offset:2048
	ds_read_b128 v[22:25], v196 offset:3072
	ds_read_b128 v[10:13], v197
	ds_read_b128 v[14:17], v197 offset:1024
	ds_read_b128 v[2:5], v197 offset:2048
	ds_read_b128 v[6:9], v197 offset:3072
	s_add_u32 s54, s30, s4
	s_addc_u32 s55, s31, s5
	s_add_u32 s56, s54, 0x30200100
	s_addc_u32 s57, s55, 0
	s_add_u32 s72, s69, s4
	s_addc_u32 s73, s70, s5
	s_cmpk_eq_i32 s4, 0x700
	s_cselect_b64 vcc, -1, 0
	s_and_b64 s[54:55], vcc, exec
	v_cndmask_b32_e32 v166, v204, v200, vcc
	s_cselect_b32 s57, s13, s57
	s_cselect_b32 s56, s12, s56
	v_cndmask_b32_e32 v171, v170, v202, vcc
	v_cndmask_b32_e32 v238, v168, v201, vcc
	v_cndmask_b32_e32 v173, v172, v203, vcc
	s_cselect_b32 s55, s49, s73
	s_cselect_b32 s54, s68, s72
	v_lshl_add_u64 v[230:231], v[176:177], 0, s[4:5]
	s_add_i32 m0, s11, 0xc000
	ds_read_b128 v[178:181], v198
	ds_read_b128 v[182:185], v198 offset:1024
	ds_read_b128 v[206:209], v198 offset:2048
	ds_read_b128 v[210:213], v198 offset:3072
	ds_read_b128 v[214:217], v198 offset:4096
	ds_read_b128 v[218:221], v198 offset:5120
	ds_read_b128 v[222:225], v198 offset:6144
	ds_read_b128 v[226:229], v198 offset:7168
	global_load_lds_dwordx4 v[230:231], off
	v_lshl_add_u64 v[230:231], v[174:175], 0, s[4:5]
	s_add_i32 m0, s11, 0xe000
	s_nop 0
	global_load_lds_dwordx4 v[230:231], off
	s_waitcnt vmcnt(8)
	s_waitcnt lgkmcnt(0)
	s_barrier
	s_setprio 1
	s_waitcnt lgkmcnt(0)
	v_mfma_scale_f32_16x16x128_f8f6f4 v[158:161], v[26:33], v[178:185], v[158:161], v199, v199 op_sel_hi:[0,0,0]
	v_mfma_scale_f32_16x16x128_f8f6f4 v[154:157], v[18:25], v[178:185], v[154:157], v199, v199 op_sel_hi:[0,0,0]
	v_mfma_scale_f32_16x16x128_f8f6f4 v[146:149], v[26:33], v[206:213], v[146:149], v199, v199 op_sel_hi:[0,0,0]
	v_mfma_scale_f32_16x16x128_f8f6f4 v[138:141], v[18:25], v[206:213], v[138:141], v199, v199 op_sel_hi:[0,0,0]
	v_mfma_scale_f32_16x16x128_f8f6f4 v[130:133], v[26:33], v[214:221], v[130:133], v199, v199 op_sel_hi:[0,0,0]
	v_mfma_scale_f32_16x16x128_f8f6f4 v[122:125], v[18:25], v[214:221], v[122:125], v199, v199 op_sel_hi:[0,0,0]
	v_mfma_scale_f32_16x16x128_f8f6f4 v[114:117], v[26:33], v[222:229], v[114:117], v199, v199 op_sel_hi:[0,0,0]
	v_mfma_scale_f32_16x16x128_f8f6f4 v[106:109], v[18:25], v[222:229], v[106:109], v199, v199 op_sel_hi:[0,0,0]
	s_setprio 0
	s_setprio 1
	v_mfma_scale_f32_16x16x128_f8f6f4 v[150:153], v[10:17], v[178:185], v[150:153], v199, v199 op_sel_hi:[0,0,0]
	v_mfma_scale_f32_16x16x128_f8f6f4 v[142:145], v[2:9], v[178:185], v[142:145], v199, v199 op_sel_hi:[0,0,0]
	v_mfma_scale_f32_16x16x128_f8f6f4 v[134:137], v[10:17], v[206:213], v[134:137], v199, v199 op_sel_hi:[0,0,0]
	v_mfma_scale_f32_16x16x128_f8f6f4 v[126:129], v[2:9], v[206:213], v[126:129], v199, v199 op_sel_hi:[0,0,0]
	v_mfma_scale_f32_16x16x128_f8f6f4 v[118:121], v[10:17], v[214:221], v[118:121], v199, v199 op_sel_hi:[0,0,0]
	v_mfma_scale_f32_16x16x128_f8f6f4 v[110:113], v[2:9], v[214:221], v[110:113], v199, v199 op_sel_hi:[0,0,0]
	v_mfma_scale_f32_16x16x128_f8f6f4 v[102:105], v[10:17], v[222:229], v[102:105], v199, v199 op_sel_hi:[0,0,0]
	v_mfma_scale_f32_16x16x128_f8f6f4 v[98:101], v[2:9], v[222:229], v[98:101], v199, v199 op_sel_hi:[0,0,0]
	s_setprio 0
	s_barrier
	s_add_i32 s72, s60, s1
	v_lshl_add_u64 v[178:179], s[54:55], 0, v[164:165]
	s_mov_b32 m0, s72
	ds_read_b128 v[206:209], v198 offset:16384
	ds_read_b128 v[210:213], v198 offset:17408
	ds_read_b128 v[214:217], v198 offset:18432
	ds_read_b128 v[218:221], v198 offset:19456
	ds_read_b128 v[222:225], v198 offset:20480
	ds_read_b128 v[226:229], v198 offset:21504
	ds_read_b128 v[230:233], v198 offset:22528
	ds_read_b128 v[234:237], v198 offset:23552
	global_load_lds_dwordx4 v[178:179], off
	s_add_i32 m0, s72, 0x2000
	s_add_u32 s72, s54, 0x40000
	v_lshl_add_u64 v[180:181], s[54:55], 0, v[162:163]
	s_addc_u32 s73, s55, 0
	s_add_i32 s74, s61, s1
	global_load_lds_dwordx4 v[180:181], off
	v_lshl_add_u64 v[182:183], s[72:73], 0, v[164:165]
	s_mov_b32 m0, s74
	v_mov_b32_e32 v239, v167
	global_load_lds_dwordx4 v[182:183], off
	v_lshl_add_u64 v[182:183], s[72:73], 0, v[162:163]
	s_add_i32 m0, s74, 0x2000
	v_lshl_add_u64 v[184:185], s[56:57], 0, v[166:167]
	global_load_lds_dwordx4 v[182:183], off
	s_mov_b32 m0, s11
	v_lshl_add_u64 v[182:183], s[56:57], 0, v[238:239]
	global_load_lds_dwordx4 v166, s[56:57]
	s_mov_b32 m0, s33
	s_nop 0
	global_load_lds_dwordx4 v238, s[56:57]
	s_waitcnt vmcnt(8)
	s_waitcnt lgkmcnt(0)
	s_barrier
	s_setprio 1
	s_waitcnt lgkmcnt(0)
	v_mfma_scale_f32_16x16x128_f8f6f4 v[94:97], v[26:33], v[206:213], v[94:97], v199, v199 op_sel_hi:[0,0,0]
	v_mfma_scale_f32_16x16x128_f8f6f4 v[90:93], v[18:25], v[206:213], v[90:93], v199, v199 op_sel_hi:[0,0,0]
	v_mfma_scale_f32_16x16x128_f8f6f4 v[82:85], v[26:33], v[214:221], v[82:85], v199, v199 op_sel_hi:[0,0,0]
	v_mfma_scale_f32_16x16x128_f8f6f4 v[74:77], v[18:25], v[214:221], v[74:77], v199, v199 op_sel_hi:[0,0,0]
	v_mfma_scale_f32_16x16x128_f8f6f4 v[66:69], v[26:33], v[222:229], v[66:69], v199, v199 op_sel_hi:[0,0,0]
	v_mfma_scale_f32_16x16x128_f8f6f4 v[58:61], v[18:25], v[222:229], v[58:61], v199, v199 op_sel_hi:[0,0,0]
	v_mfma_scale_f32_16x16x128_f8f6f4 v[50:53], v[26:33], v[230:237], v[50:53], v199, v199 op_sel_hi:[0,0,0]
	v_mfma_scale_f32_16x16x128_f8f6f4 v[42:45], v[18:25], v[230:237], v[42:45], v199, v199 op_sel_hi:[0,0,0]
	s_setprio 0
	s_setprio 1
	v_mfma_scale_f32_16x16x128_f8f6f4 v[86:89], v[10:17], v[206:213], v[86:89], v199, v199 op_sel_hi:[0,0,0]
	v_mfma_scale_f32_16x16x128_f8f6f4 v[78:81], v[2:9], v[206:213], v[78:81], v199, v199 op_sel_hi:[0,0,0]
	v_mfma_scale_f32_16x16x128_f8f6f4 v[70:73], v[10:17], v[214:221], v[70:73], v199, v199 op_sel_hi:[0,0,0]
	v_mfma_scale_f32_16x16x128_f8f6f4 v[62:65], v[2:9], v[214:221], v[62:65], v199, v199 op_sel_hi:[0,0,0]
	v_mfma_scale_f32_16x16x128_f8f6f4 v[54:57], v[10:17], v[222:229], v[54:57], v199, v199 op_sel_hi:[0,0,0]
	v_mfma_scale_f32_16x16x128_f8f6f4 v[46:49], v[2:9], v[222:229], v[46:49], v199, v199 op_sel_hi:[0,0,0]
	v_mfma_scale_f32_16x16x128_f8f6f4 v[38:41], v[10:17], v[230:237], v[38:41], v199, v199 op_sel_hi:[0,0,0]
	v_mfma_scale_f32_16x16x128_f8f6f4 v[34:37], v[2:9], v[230:237], v[34:37], v199, v199 op_sel_hi:[0,0,0]
	s_setprio 0
	s_barrier
; #define PG8_STAGE(bufoff, gbase, voff) do { _Pragma("unroll") for (int _i = 0; _i < 2; ++_i) \
;         __builtin_amdgcn_global_load_lds((const unsigned*)((const char*)(gbase) + (voff)[_i]), (PG8_LAS unsigned*)(lds + (bufoff) + ldsw + _i * 8192), 16, 0, 0); } while (0)
; #define PG8_LDA(dst, b, h) do { _Pragma("unroll") for (int m = 0; m < 4; ++m) _Pragma("unroll") for (int k = 0; k < 2; ++k) dst[m][k] = *(const PG8_LAS bf16x8*)(lds + PG8_SA(b, h) + aoff + m * 2048 + k * 1024); } while (0)
; #define PG8_LDB(dst, b, h) do { _Pragma("unroll") for (int n = 0; n < 2; ++n) _Pragma("unroll") for (int k = 0; k < 2; ++k) dst[n][k] = *(const PG8_LAS bf16x8*)(lds + PG8_SB(b, h) + boff + n * 2048 + k * 1024); } while (0)
; #define PG8_WAIT_V(n) asm volatile("s_waitcnt vmcnt(" #n ")" ::: "memory")
; #define PG8_WAIT_L(n) asm volatile("s_waitcnt lgkmcnt(" #n ")" ::: "memory")
; #define PG8_BAR __builtin_amdgcn_s_barrier()
; #define PG8_SCHED __builtin_amdgcn_sched_barrier(0)
; template <class Epi, class Sched, bool ALIGN_EPI = false, bool SP2 = false, bool F8 = false, bool GATHER = false>
; __device__ __forceinline__ void gemm_phase(PG8_LAS unsigned char* lds, const Gemm g, const Sched& S, const Epi& E) {
;     ...
;             PG8_LDB(B0, 1, 0); PG8_LDB(B1, 1, 1); PG8_SCHED; PG8_LDA(At, 1, 0); PG8_STAGE(PG8_SA(0, 1), a2, s1);
;             PG8_WAIT_V(8); PG8_WAIT_L(0); PG8_BAR; PG8_MMA(0, 0, At, B0); PG8_MMA(0, 1, At, B1); PG8_BAR; PG8_SCHED;
;             PG8_LDA(At, 1, 1); PG8_STAGE(PG8_SB(1, 0), b3, voffB); PG8_STAGE(PG8_SB(1, 1), b3 + hstep, voffB); PG8_STAGE(PG8_SA(1, 0), a3, s0);
;             PG8_WAIT_V(8); PG8_WAIT_L(0); PG8_BAR; PG8_MMA(1, 0, At, B0); PG8_MMA(1, 1, At, B1); PG8_BAR; PG8_SCHED;
	s_add_i32 s72, 0, 0x18000
	s_add_i32 s73, 0, 0x1c000
	v_add_u32_e32 v14, s72, v194
	v_add_u32_e32 v30, s73, v194
	ds_read_b128 v[2:5], v14
	ds_read_b128 v[6:9], v14 offset:1024
	ds_read_b128 v[10:13], v14 offset:2048
	ds_read_b128 v[14:17], v14 offset:3072
	ds_read_b128 v[18:21], v30
	ds_read_b128 v[22:25], v30 offset:1024
	ds_read_b128 v[26:29], v30 offset:2048
	ds_read_b128 v[30:33], v30 offset:3072
	s_mov_b32 m0, s34
	ds_read_b128 v[206:209], v198 offset:32768
	ds_read_b128 v[210:213], v198 offset:33792
	ds_read_b128 v[214:217], v198 offset:34816
	ds_read_b128 v[218:221], v198 offset:35840
	ds_read_b128 v[222:225], v198 offset:36864
	ds_read_b128 v[226:229], v198 offset:37888
	ds_read_b128 v[230:233], v198 offset:38912
	ds_read_b128 v[234:237], v198 offset:39936
	global_load_lds_dwordx4 v171, s[56:57]
	s_mov_b32 m0, s35
	s_nop 0
	global_load_lds_dwordx4 v173, s[56:57]
	s_waitcnt vmcnt(8)
	s_waitcnt lgkmcnt(0)
	s_barrier
	s_setprio 1
	s_waitcnt lgkmcnt(0)
	v_mfma_scale_f32_16x16x128_f8f6f4 v[158:161], v[2:9], v[206:213], v[158:161], v199, v199 op_sel_hi:[0,0,0]
	v_mfma_scale_f32_16x16x128_f8f6f4 v[154:157], v[10:17], v[206:213], v[154:157], v199, v199 op_sel_hi:[0,0,0]
	v_mfma_scale_f32_16x16x128_f8f6f4 v[146:149], v[2:9], v[214:221], v[146:149], v199, v199 op_sel_hi:[0,0,0]
	v_mfma_scale_f32_16x16x128_f8f6f4 v[138:141], v[10:17], v[214:221], v[138:141], v199, v199 op_sel_hi:[0,0,0]
	v_mfma_scale_f32_16x16x128_f8f6f4 v[130:133], v[2:9], v[222:229], v[130:133], v199, v199 op_sel_hi:[0,0,0]
	v_mfma_scale_f32_16x16x128_f8f6f4 v[122:125], v[10:17], v[222:229], v[122:125], v199, v199 op_sel_hi:[0,0,0]
	v_mfma_scale_f32_16x16x128_f8f6f4 v[114:117], v[2:9], v[230:237], v[114:117], v199, v199 op_sel_hi:[0,0,0]
	v_mfma_scale_f32_16x16x128_f8f6f4 v[106:109], v[10:17], v[230:237], v[106:109], v199, v199 op_sel_hi:[0,0,0]
	s_setprio 0
	s_setprio 1
	v_mfma_scale_f32_16x16x128_f8f6f4 v[150:153], v[18:25], v[206:213], v[150:153], v199, v199 op_sel_hi:[0,0,0]
	v_mfma_scale_f32_16x16x128_f8f6f4 v[142:145], v[26:33], v[206:213], v[142:145], v199, v199 op_sel_hi:[0,0,0]
	v_mfma_scale_f32_16x16x128_f8f6f4 v[134:137], v[18:25], v[214:221], v[134:137], v199, v199 op_sel_hi:[0,0,0]
	v_mfma_scale_f32_16x16x128_f8f6f4 v[126:129], v[26:33], v[214:221], v[126:129], v199, v199 op_sel_hi:[0,0,0]
	v_mfma_scale_f32_16x16x128_f8f6f4 v[118:121], v[18:25], v[222:229], v[118:121], v199, v199 op_sel_hi:[0,0,0]
	v_mfma_scale_f32_16x16x128_f8f6f4 v[110:113], v[26:33], v[222:229], v[110:113], v199, v199 op_sel_hi:[0,0,0]
	v_mfma_scale_f32_16x16x128_f8f6f4 v[102:105], v[18:25], v[230:237], v[102:105], v199, v199 op_sel_hi:[0,0,0]
	v_mfma_scale_f32_16x16x128_f8f6f4 v[98:101], v[26:33], v[230:237], v[98:101], v199, v199 op_sel_hi:[0,0,0]
	s_setprio 0
	s_barrier
	s_add_i32 s56, s72, s1
	v_lshl_add_u64 v[178:179], v[178:179], 0, s[22:23]
	s_mov_b32 m0, s56
	ds_read_b128 v[206:209], v198 offset:49152
	ds_read_b128 v[210:213], v198 offset:50176
	ds_read_b128 v[214:217], v198 offset:51200
	ds_read_b128 v[218:221], v198 offset:52224
	ds_read_b128 v[222:225], v198 offset:53248
	ds_read_b128 v[226:229], v198 offset:54272
	ds_read_b128 v[230:233], v198 offset:55296
	ds_read_b128 v[234:237], v198 offset:56320
	global_load_lds_dwordx4 v[178:179], off
	s_add_i32 m0, s56, 0x2000
	s_add_u32 s54, s54, 0x40080
	v_lshl_add_u64 v[178:179], v[180:181], 0, s[22:23]
	s_addc_u32 s55, s55, 0
	s_add_i32 s56, s73, s1
	global_load_lds_dwordx4 v[178:179], off
	v_lshl_add_u64 v[178:179], s[54:55], 0, v[164:165]
	s_mov_b32 m0, s56
	s_nop 0
	global_load_lds_dwordx4 v[178:179], off
	v_lshl_add_u64 v[178:179], s[54:55], 0, v[162:163]
	s_add_i32 m0, s56, 0x2000
	s_nop 0
	global_load_lds_dwordx4 v[178:179], off
	v_lshl_add_u64 v[178:179], v[184:185], 0, s[22:23]
	s_mov_b32 m0, s58
	s_nop 0
	global_load_lds_dwordx4 v[178:179], off
	v_lshl_add_u64 v[178:179], v[182:183], 0, s[22:23]
	s_mov_b32 m0, s59
	s_nop 0
	global_load_lds_dwordx4 v[178:179], off
	s_waitcnt vmcnt(8)
	s_waitcnt lgkmcnt(0)
	s_barrier
	s_setprio 1
	s_waitcnt lgkmcnt(0)
	v_mfma_scale_f32_16x16x128_f8f6f4 v[94:97], v[2:9], v[206:213], v[94:97], v199, v199 op_sel_hi:[0,0,0]
	v_mfma_scale_f32_16x16x128_f8f6f4 v[90:93], v[10:17], v[206:213], v[90:93], v199, v199 op_sel_hi:[0,0,0]
	v_mfma_scale_f32_16x16x128_f8f6f4 v[82:85], v[2:9], v[214:221], v[82:85], v199, v199 op_sel_hi:[0,0,0]
	v_mfma_scale_f32_16x16x128_f8f6f4 v[74:77], v[10:17], v[214:221], v[74:77], v199, v199 op_sel_hi:[0,0,0]
	v_mfma_scale_f32_16x16x128_f8f6f4 v[66:69], v[2:9], v[222:229], v[66:69], v199, v199 op_sel_hi:[0,0,0]
	v_mfma_scale_f32_16x16x128_f8f6f4 v[58:61], v[10:17], v[222:229], v[58:61], v199, v199 op_sel_hi:[0,0,0]
	v_mfma_scale_f32_16x16x128_f8f6f4 v[50:53], v[2:9], v[230:237], v[50:53], v199, v199 op_sel_hi:[0,0,0]
	v_mfma_scale_f32_16x16x128_f8f6f4 v[42:45], v[10:17], v[230:237], v[42:45], v199, v199 op_sel_hi:[0,0,0]
	s_setprio 0
	s_setprio 1
	v_mfma_scale_f32_16x16x128_f8f6f4 v[86:89], v[18:25], v[206:213], v[86:89], v199, v199 op_sel_hi:[0,0,0]
	v_mfma_scale_f32_16x16x128_f8f6f4 v[78:81], v[26:33], v[206:213], v[78:81], v199, v199 op_sel_hi:[0,0,0]
	v_mfma_scale_f32_16x16x128_f8f6f4 v[70:73], v[18:25], v[214:221], v[70:73], v199, v199 op_sel_hi:[0,0,0]
	v_mfma_scale_f32_16x16x128_f8f6f4 v[62:65], v[26:33], v[214:221], v[62:65], v199, v199 op_sel_hi:[0,0,0]
	v_mfma_scale_f32_16x16x128_f8f6f4 v[54:57], v[18:25], v[222:229], v[54:57], v199, v199 op_sel_hi:[0,0,0]
	v_mfma_scale_f32_16x16x128_f8f6f4 v[46:49], v[26:33], v[222:229], v[46:49], v199, v199 op_sel_hi:[0,0,0]
	v_mfma_scale_f32_16x16x128_f8f6f4 v[38:41], v[18:25], v[230:237], v[38:41], v199, v199 op_sel_hi:[0,0,0]
	v_mfma_scale_f32_16x16x128_f8f6f4 v[34:37], v[26:33], v[230:237], v[34:37], v199, v199 op_sel_hi:[0,0,0]
	s_setprio 0
	s_barrier
	s_add_i32 s71, s71, 2
	s_add_u32 s4, s4, 0x100
	s_addc_u32 s5, s5, 0
	s_cmp_gt_u32 s71, 13
	s_cbranch_scc0 .LBB0_1073
	s_nop 15
	s_nop 7
	s_and_b64 vcc, exec, s[36:37]
	s_cbranch_vccz .LBB0_1076
	s_barrier
